# phase H router: LDS weight reads software-pipelined two pairs deep (upper table half addressed base+offset to free registers)
# speedup vs baseline: 1.0015x; 1.0015x over previous
; #define LAS __attribute__((address_space(3)))
; __device__ __forceinline__ float bflo(unsigned w) { return __uint_as_float(w << 16); }
; __device__ __forceinline__ float bfhi(unsigned w) { return __uint_as_float(w & 0xffff0000u); }
; #define H_MLOAD(dst, jj) do { dst[0] = *(const f32x4*)(gp + (jj) * 512); dst[1] = *(const f32x4*)(gp + (jj) * 512 + 4); dst[2] = *(const f32x4*)(m + 4 * DM + (jj) * 512); dst[3] = *(const f32x4*)(m + 4 * DM + (jj) * 512 + 4); \
;             dst[4] = *(const f32x4*)(m + 3 * DM + (jj) * 512); dst[5] = *(const f32x4*)(m + 3 * DM + (jj) * 512 + 4); } while (0)
; __device__ __forceinline__ void ph_norm2_router(const Params& p, int l, LAS unsigned char* lds) {
;     ...
;         const int row = it * 8 + wave; const int rr = row < NLAT ? (row >> 11) : 4;
;         const float* m = mod + (size_t)rr * 12288 + lane * 8; const float* gp = n2g + lane * 8;
;         u32x4 xv[4];
; #pragma unroll
;         for (int j = 0; j < 4; ++j) xv[j] = xn[j];
;         { const int itn = it + (int)gridDim.x; if (itn < nrows / 8) { const bf16_t* xr = (const bf16_t*)(ws + WS_XB) + (size_t)(itn * 8 + wave) * DM + lane * 8;
; #pragma unroll
;             for (int j = 0; j < 4; ++j) xn[j] = *(const u32x4*)(xr + j * 512); } }
;         float x[4][8]; float ss = 0.f;
; #pragma unroll
;         for (int j = 0; j < 4; ++j) { x[j][0] = bflo(xv[j].x); x[j][1] = bfhi(xv[j].x); x[j][2] = bflo(xv[j].y); x[j][3] = bfhi(xv[j].y); x[j][4] = bflo(xv[j].z); x[j][5] = bfhi(xv[j].z); x[j][6] = bflo(xv[j].w); x[j][7] = bfhi(xv[j].w);
; #pragma unroll
;             for (int i = 0; i < 8; ++i) ss += x[j][i] * x[j][i]; }
;         ss = wave_sum(ss); const float rinv = rsqrtf(ss * (1.0f / DM) + EPS);
;         bf16_t* orow = (bf16_t*)(ws + WS_H) + (size_t)row * DM + lane * 8;
;         f32x4 lg[4];
; #pragma unroll
;         for (int e4 = 0; e4 < 4; ++e4) lg[e4] = (f32x4){0.f, 0.f, 0.f, 0.f};
;         f32x4 mv[2][6];
;     ...
;         H_MLOAD(mv[0], 0);
;     ...
;                 for (int e4 = 0; e4 < 4; ++e4) { const f32x4 w0 = *(const LAS f32x4*)(lds + (size_t)(((e4 * 8 + i2) * 256 + j * 64 + lane) * 16)); const f32x4 w1 = *(const LAS f32x4*)(lds + (size_t)(((e4 * 8 + i2 + 1) * 256 + j * 64 + lane) * 16));
.LBB0_1760:
	v_readlane_b32 s0, v253, 61
	global_load_dwordx4 v[46:49], v[68:69], off offset:16
	global_load_dwordx4 v[54:57], v[68:69], off
	v_add_u32_e32 v80, s0, v93
	v_min_i32_e32 v18, 0x2000, v80
	v_ashrrev_i32_e32 v18, 11, v18
	v_mul_hi_i32_i24_e32 v19, 0xc000, v18
	v_mul_i32_i24_e32 v18, 0xc000, v18
	v_lshl_add_u64 v[58:59], v[66:67], 0, v[18:19]
	s_mov_b64 s[0:1], 0x8000
	v_lshl_add_u64 v[26:27], v[58:59], 0, s[0:1]
	s_mov_b32 s0, 0x8000
	v_add_co_u32_e32 v28, vcc, s0, v58
	s_mov_b32 s0, 0x9000
	s_nop 0
	v_addc_co_u32_e32 v29, vcc, 0, v59, vcc
	v_add_co_u32_e32 v94, vcc, s0, v58
	s_mov_b64 s[0:1], 0x6000
	s_nop 0
	v_addc_co_u32_e32 v95, vcc, 0, v59, vcc
	v_lshl_add_u64 v[30:31], v[58:59], 0, s[0:1]
	s_movk_i32 s0, 0x6000
	v_add_co_u32_e32 v32, vcc, s0, v58
	s_movk_i32 s0, 0x7000
	s_nop 0
	v_addc_co_u32_e32 v33, vcc, 0, v59, vcc
	v_add_co_u32_e32 v96, vcc, s0, v58
	v_lshlrev_b32_e32 v236, 16, v50
	s_nop 0
	v_addc_co_u32_e32 v97, vcc, 0, v59, vcc
	global_load_dwordx4 v[60:63], v[94:95], off offset:-4096
	global_load_dwordx4 v[194:197], v[96:97], off offset:-4096
	s_waitcnt lgkmcnt(0)
	global_load_dwordx4 v[18:21], v[68:69], off offset:2064
	global_load_dwordx4 v[22:25], v[68:69], off offset:2048
	global_load_dwordx4 v[106:109], v[26:27], off offset:16
	global_load_dwordx4 v[118:121], v[28:29], off offset:2048
	v_and_b32_e32 v237, 0xffff0000, v50
	v_lshlrev_b32_e32 v214, 16, v51
	v_and_b32_e32 v215, 0xffff0000, v51
	v_pk_mul_f32 v[208:209], v[236:237], v[236:237]
	s_mov_b64 s[0:1], 0x8800
	v_pk_mul_f32 v[116:117], v[214:215], v[214:215]
	v_add_f32_e32 v81, v208, v209
	v_lshl_add_u64 v[64:65], v[58:59], 0, s[0:1]
	s_mov_b64 s[0:1], 0x6800
	v_lshlrev_b32_e32 v212, 16, v52
	v_and_b32_e32 v213, 0xffff0000, v52
	v_add_f32_e32 v81, v116, v81
	v_lshl_add_u64 v[26:27], v[58:59], 0, s[0:1]
	v_pk_mul_f32 v[114:115], v[212:213], v[212:213]
	v_add_f32_e32 v81, v117, v81
	global_load_dwordx4 v[198:201], v[30:31], off offset:16
	s_nop 0
	global_load_dwordx4 v[30:33], v[32:33], off offset:2048
	s_nop 0
	global_load_dwordx4 v[202:205], v[64:65], off offset:16
	s_nop 0
	global_load_dwordx4 v[26:29], v[26:27], off offset:16
	v_lshlrev_b32_e32 v64, 16, v53
	v_and_b32_e32 v65, 0xffff0000, v53
	v_add_f32_e32 v81, v114, v81
	v_pk_mul_f32 v[90:91], v[64:65], v[64:65]
	v_add_f32_e32 v81, v115, v81
	v_lshlrev_b32_e32 v112, 16, v42
	v_and_b32_e32 v113, 0xffff0000, v42
	v_add_f32_e32 v81, v90, v81
	v_lshlrev_b32_e32 v110, 16, v43
	v_and_b32_e32 v111, 0xffff0000, v43
	v_pk_mul_f32 v[42:43], v[112:113], v[112:113]
	v_add_f32_e32 v81, v91, v81
	v_add_f32_e32 v42, v42, v81
	v_pk_mul_f32 v[216:217], v[110:111], v[110:111]
	v_add_f32_e32 v42, v43, v42
	v_lshlrev_b32_e32 v52, 16, v44
	v_and_b32_e32 v53, 0xffff0000, v44
	v_add_f32_e32 v42, v216, v42
	v_lshlrev_b32_e32 v50, 16, v45
	v_and_b32_e32 v51, 0xffff0000, v45
	v_pk_mul_f32 v[44:45], v[52:53], v[52:53]
	v_add_f32_e32 v42, v217, v42
	v_add_f32_e32 v42, v44, v42
	v_pk_mul_f32 v[210:211], v[50:51], v[50:51]
	v_add_f32_e32 v42, v45, v42
	v_lshlrev_b32_e32 v104, 16, v38
	v_and_b32_e32 v105, 0xffff0000, v38
	v_add_f32_e32 v42, v210, v42
	v_lshlrev_b32_e32 v102, 16, v39
	v_and_b32_e32 v103, 0xffff0000, v39
	v_pk_mul_f32 v[38:39], v[104:105], v[104:105]
	v_add_f32_e32 v42, v211, v42
	v_add_f32_e32 v38, v38, v42
	v_pk_mul_f32 v[220:221], v[102:103], v[102:103]
	v_add_f32_e32 v38, v39, v38
	v_lshlrev_b32_e32 v100, 16, v40
	v_and_b32_e32 v101, 0xffff0000, v40
	v_add_f32_e32 v38, v220, v38
	v_lshlrev_b32_e32 v98, 16, v41
	v_and_b32_e32 v99, 0xffff0000, v41
	v_pk_mul_f32 v[40:41], v[100:101], v[100:101]
	v_add_f32_e32 v38, v221, v38
	v_add_f32_e32 v38, v40, v38
	v_pk_mul_f32 v[218:219], v[98:99], v[98:99]
	v_add_f32_e32 v38, v41, v38
	v_lshlrev_b32_e32 v88, 16, v34
	v_and_b32_e32 v89, 0xffff0000, v34
	v_add_f32_e32 v38, v218, v38
	v_lshlrev_b32_e32 v86, 16, v35
	v_and_b32_e32 v87, 0xffff0000, v35
	v_pk_mul_f32 v[34:35], v[88:89], v[88:89]
	v_add_f32_e32 v38, v219, v38
	v_add_f32_e32 v34, v34, v38
	v_pk_mul_f32 v[224:225], v[86:87], v[86:87]
	v_add_f32_e32 v34, v35, v34
	v_lshlrev_b32_e32 v84, 16, v36
	v_and_b32_e32 v85, 0xffff0000, v36
	v_add_f32_e32 v34, v224, v34
	v_lshlrev_b32_e32 v82, 16, v37
	v_and_b32_e32 v83, 0xffff0000, v37
	v_pk_mul_f32 v[36:37], v[84:85], v[84:85]
	v_add_f32_e32 v34, v225, v34
	v_add_f32_e32 v34, v36, v34
	v_pk_mul_f32 v[222:223], v[82:83], v[82:83]
	v_add_f32_e32 v34, v37, v34
	v_add_f32_e32 v34, v222, v34
	v_add_f32_e32 v34, v223, v34
	v_mov_b32_e32 v35, v34
	s_nop 1
	v_permlane32_swap_b32_e32 v35, v34
	v_ashrrev_i32_e32 v81, 31, v80
	s_mov_b64 s[0:1], 0x9000
	s_waitcnt vmcnt(5)
	v_pk_add_f32 v[240:241], v[108:109], 1.0 op_sel_hi:[1,0]
	v_pk_add_f32 v[238:239], v[60:61], 1.0 op_sel_hi:[1,0]
	s_waitcnt lgkmcnt(0)
	v_add_f32_e32 v36, v34, v35
	v_mov_b32_e32 v37, v36
	s_nop 1
	v_permlane16_swap_b32_e32 v37, v36
	v_lshlrev_b64 v[34:35], 12, v[80:81]
	v_lshl_add_u64 v[90:91], v[72:73], 0, v[34:35]
	v_pk_add_f32 v[34:35], v[106:107], 1.0 op_sel_hi:[1,0]
	s_waitcnt vmcnt(4)
	v_pk_add_f32 v[116:117], v[120:121], 1.0 op_sel_hi:[1,0]
	s_waitcnt lgkmcnt(0)
	v_add_f32_e32 v38, v36, v37
	s_nop 1
	v_mov_b32_dpp v39, v38 row_ror:8 row_mask:0xf bank_mask:0xf
	v_pk_add_f32 v[36:37], v[62:63], 1.0 op_sel_hi:[1,0]
	ds_read_b128 v[42:45], v128
	ds_read_b128 v[60:63], v128 offset:4096
	ds_read_b128 v[208:211], v128 offset:32768
	ds_read_b128 v[216:219], v128 offset:36864
	ds_read_b128 v[220:223], v129
	ds_read_b128 v[224:227], v129 offset:4096
	ds_read_b128 v[228:231], v129 offset:32768
	ds_read_b128 v[232:235], v129 offset:36864
	s_waitcnt vmcnt(1)
	v_pk_add_f32 v[114:115], v[202:203], 1.0 op_sel_hi:[1,0]
	s_waitcnt lgkmcnt(8)
; #define LAS __attribute__((address_space(3)))
; __device__ __forceinline__ unsigned cvt_pk_bf16(float lo, float hi) { const f32x2 v = {lo, hi}; const bf16x2_t b = __builtin_convertvector(v, bf16x2_t); return __builtin_bit_cast(unsigned, b); }
; #define H_MLOAD(dst, jj) do { dst[0] = *(const f32x4*)(gp + (jj) * 512); dst[1] = *(const f32x4*)(gp + (jj) * 512 + 4); dst[2] = *(const f32x4*)(m + 4 * DM + (jj) * 512); dst[3] = *(const f32x4*)(m + 4 * DM + (jj) * 512 + 4); \
;             dst[4] = *(const f32x4*)(m + 3 * DM + (jj) * 512); dst[5] = *(const f32x4*)(m + 3 * DM + (jj) * 512 + 4); } while (0)
; __device__ __forceinline__ void ph_norm2_router(const Params& p, int l, LAS unsigned char* lds) {
;     ...
;         for (int j = 0; j < 4; ++j) {
;             if (j < 3) H_MLOAD(mv[(j + 1) & 1], j + 1);
;             const f32x4 ga = mv[j & 1][0], gb = mv[j & 1][1], sa = mv[j & 1][2], sb = mv[j & 1][3], ha = mv[j & 1][4], hb = mv[j & 1][5];
;             float y[8];
; #pragma unroll
;             for (int i = 0; i < 8; ++i) y[i] = x[j][i] * rinv * (i < 4 ? ga[i] : gb[i - 4]) * (1.0f + (i < 4 ? sa[i] : sb[i - 4])) + (i < 4 ? ha[i] : hb[i - 4]);
;             u32x4 h; h.x = cvt_pk_bf16(y[0], y[1]); h.y = cvt_pk_bf16(y[2], y[3]); h.z = cvt_pk_bf16(y[4], y[5]); h.w = cvt_pk_bf16(y[6], y[7]);
;             *(u32x4*)(orow + j * 512) = h;
; #pragma unroll
;             for (int i2 = 0; i2 < 8; i2 += 2) {
; #pragma unroll
;                 for (int e4 = 0; e4 < 4; ++e4) { const f32x4 w0 = *(const LAS f32x4*)(lds + (size_t)(((e4 * 8 + i2) * 256 + j * 64 + lane) * 16)); const f32x4 w1 = *(const LAS f32x4*)(lds + (size_t)(((e4 * 8 + i2 + 1) * 256 + j * 64 + lane) * 16));
;                     lg[e4] = __builtin_elementwise_fma(w0, (f32x4){y[i2], y[i2], y[i2], y[i2]}, lg[e4]); lg[e4] = __builtin_elementwise_fma(w1, (f32x4){y[i2 + 1], y[i2 + 1], y[i2 + 1], y[i2 + 1]}, lg[e4]); }
;                 __builtin_amdgcn_sched_barrier(0); } }
	v_add_f32_e32 v38, v38, v39
	s_nop 1
	v_mov_b32_dpp v39, v38 row_shl:4 row_mask:0xf bank_mask:0x5
	v_mov_b32_dpp v39, v38 row_shr:4 row_mask:0xf bank_mask:0xa
	v_pk_add_f32 v[118:119], v[118:119], 1.0 op_sel_hi:[1,0]
	v_pk_add_f32 v[120:121], v[204:205], 1.0 op_sel_hi:[1,0]
	s_waitcnt lgkmcnt(0)
	v_add_f32_e32 v40, v38, v39
	s_nop 1
	v_mov_b32_dpp v41, v40 quad_perm:[2,3,0,1] row_mask:0xf bank_mask:0xf
	v_lshl_add_u64 v[38:39], v[58:59], 0, s[0:1]
	s_mov_b64 s[0:1], 0x7000
	s_waitcnt lgkmcnt(0)
	v_add_f32_e32 v92, v40, v41
	s_nop 1
	v_mov_b32_dpp v106, v92 quad_perm:[1,0,3,2] row_mask:0xf bank_mask:0xf
	v_lshl_add_u64 v[40:41], v[58:59], 0, s[0:1]
	s_mov_b32 s0, 0x800000
	s_waitcnt lgkmcnt(0)
	v_add_f32_e32 v92, v92, v106
	v_fmamk_f32 v92, v92, 0x3a000000, v246
	v_mul_f32_e32 v106, 0x4b800000, v92
	v_cmp_gt_f32_e32 vcc, s0, v92
	s_mov_b64 s[0:1], 0x9800
	s_nop 0
	v_cndmask_b32_e32 v92, v92, v106, vcc
	v_rsq_f32_e32 v92, v92
	v_lshl_add_u64 v[106:107], v[58:59], 0, s[0:1]
	s_mov_b64 s[0:1], 0x7800
	v_lshl_add_u64 v[108:109], v[58:59], 0, s[0:1]
	v_mul_f32_e32 v58, 0x45800000, v92
	v_cndmask_b32_e32 v92, v92, v58, vcc
	v_pk_mul_f32 v[58:59], v[92:93], v[236:237] op_sel_hi:[0,1]
	v_pk_mul_f32 v[54:55], v[54:55], v[58:59]
	v_pk_mul_f32 v[58:59], v[92:93], v[214:215] op_sel_hi:[0,1]
	v_pk_mul_f32 v[56:57], v[56:57], v[58:59]
	v_pk_fma_f32 v[54:55], v[238:239], v[54:55], v[194:195]
	v_pk_fma_f32 v[56:57], v[36:37], v[56:57], v[196:197]
	v_pk_mul_f32 v[36:37], v[92:93], v[212:213] op_sel_hi:[0,1]
	v_pk_mul_f32 v[36:37], v[46:47], v[36:37]
	v_pk_fma_f32 v[42:43], v[42:43], v[54:55], 0 op_sel_hi:[1,0,0]
	v_pk_fma_f32 v[36:37], v[34:35], v[36:37], v[198:199]
	v_pk_mul_f32 v[34:35], v[92:93], v[64:65] op_sel_hi:[0,1]
	v_pk_fma_f32 v[44:45], v[44:45], v[54:55], 0 op_sel_hi:[1,0,0]
	v_pk_mul_f32 v[34:35], v[48:49], v[34:35]
	v_pk_fma_f32 v[58:59], v[62:63], v[54:55], v[44:45] op_sel:[0,1,0]
	v_pk_fma_f32 v[60:61], v[60:61], v[54:55], v[42:43] op_sel:[0,1,0]
	v_pk_fma_f32 v[42:43], v[208:209], v[54:55], 0 op_sel_hi:[1,0,0]
	v_pk_fma_f32 v[44:45], v[210:211], v[54:55], 0 op_sel_hi:[1,0,0]
	v_pk_fma_f32 v[34:35], v[240:241], v[34:35], v[200:201]
	v_pk_fma_f32 v[62:63], v[218:219], v[54:55], v[44:45] op_sel:[0,1,0]
	v_pk_fma_f32 v[64:65], v[216:217], v[54:55], v[42:43] op_sel:[0,1,0]
	v_pk_fma_f32 v[42:43], v[220:221], v[54:55], 0 op_sel_hi:[1,0,0]
	v_pk_fma_f32 v[44:45], v[222:223], v[54:55], 0 op_sel_hi:[1,0,0]
	v_cvt_pk_bf16_f32 v46, v54, v55
	v_cvt_pk_bf16_f32 v47, v56, v57
	v_cvt_pk_bf16_f32 v48, v36, v37
	v_cvt_pk_bf16_f32 v49, v34, v35
	v_pk_fma_f32 v[194:195], v[226:227], v[54:55], v[44:45] op_sel:[0,1,0]
	v_pk_fma_f32 v[196:197], v[224:225], v[54:55], v[42:43] op_sel:[0,1,0]
	v_pk_fma_f32 v[42:43], v[228:229], v[54:55], 0 op_sel_hi:[1,0,0]
	v_pk_fma_f32 v[44:45], v[230:231], v[54:55], 0 op_sel_hi:[1,0,0]
	global_store_dwordx4 v[90:91], v[46:49], off
	v_pk_fma_f32 v[198:199], v[234:235], v[54:55], v[44:45] op_sel:[0,1,0]
	v_pk_fma_f32 v[54:55], v[232:233], v[54:55], v[42:43] op_sel:[0,1,0]
	ds_read_b128 v[42:45], v128 offset:8192
	ds_read_b128 v[46:49], v128 offset:12288
	ds_read_b128 v[130:133], v128 offset:40960
	ds_read_b128 v[134:137], v128 offset:45056
	s_waitcnt lgkmcnt(3)
	v_pk_fma_f32 v[42:43], v[42:43], v[56:57], v[60:61] op_sel_hi:[1,0,1]
	v_pk_fma_f32 v[44:45], v[44:45], v[56:57], v[58:59] op_sel_hi:[1,0,1]
	s_waitcnt lgkmcnt(2)
	v_pk_fma_f32 v[60:61], v[46:47], v[56:57], v[42:43] op_sel:[0,1,0]
	v_pk_fma_f32 v[58:59], v[48:49], v[56:57], v[44:45] op_sel:[0,1,0]
	ds_read_b128 v[42:45], v129 offset:8192
	ds_read_b128 v[46:49], v129 offset:12288
	s_waitcnt lgkmcnt(3)
	v_pk_fma_f32 v[130:131], v[130:131], v[56:57], v[64:65] op_sel_hi:[1,0,1]
	v_pk_fma_f32 v[132:133], v[132:133], v[56:57], v[62:63] op_sel_hi:[1,0,1]
	s_waitcnt lgkmcnt(2)
	v_pk_fma_f32 v[64:65], v[134:135], v[56:57], v[130:131] op_sel:[0,1,0]
	v_pk_fma_f32 v[62:63], v[136:137], v[56:57], v[132:133] op_sel:[0,1,0]
	ds_read_b128 v[130:133], v129 offset:40960
	ds_read_b128 v[134:137], v129 offset:45056
	s_waitcnt lgkmcnt(3)
	v_pk_fma_f32 v[42:43], v[42:43], v[56:57], v[196:197] op_sel_hi:[1,0,1]
	v_pk_fma_f32 v[44:45], v[44:45], v[56:57], v[194:195] op_sel_hi:[1,0,1]
	s_waitcnt lgkmcnt(2)
	v_pk_fma_f32 v[196:197], v[46:47], v[56:57], v[42:43] op_sel:[0,1,0]
	v_pk_fma_f32 v[194:195], v[48:49], v[56:57], v[44:45] op_sel:[0,1,0]
	ds_read_b128 v[42:45], v128 offset:16384
	ds_read_b128 v[46:49], v128 offset:20480
	s_waitcnt lgkmcnt(3)
	v_pk_fma_f32 v[130:131], v[130:131], v[56:57], v[54:55] op_sel_hi:[1,0,1]
	v_pk_fma_f32 v[132:133], v[132:133], v[56:57], v[198:199] op_sel_hi:[1,0,1]
	s_waitcnt lgkmcnt(2)
	v_pk_fma_f32 v[54:55], v[136:137], v[56:57], v[132:133] op_sel:[0,1,0]
	v_pk_fma_f32 v[56:57], v[134:135], v[56:57], v[130:131] op_sel:[0,1,0]
	ds_read_b128 v[130:133], v128 offset:49152
	ds_read_b128 v[134:137], v128 offset:53248
	s_waitcnt lgkmcnt(3)
	v_pk_fma_f32 v[42:43], v[42:43], v[36:37], v[60:61] op_sel_hi:[1,0,1]
	v_pk_fma_f32 v[44:45], v[44:45], v[36:37], v[58:59] op_sel_hi:[1,0,1]
	s_waitcnt lgkmcnt(2)
	v_pk_fma_f32 v[60:61], v[46:47], v[36:37], v[42:43] op_sel:[0,1,0]
	v_pk_fma_f32 v[58:59], v[48:49], v[36:37], v[44:45] op_sel:[0,1,0]
	ds_read_b128 v[42:45], v129 offset:16384
	ds_read_b128 v[46:49], v129 offset:20480
	s_waitcnt lgkmcnt(3)
	v_pk_fma_f32 v[130:131], v[130:131], v[36:37], v[64:65] op_sel_hi:[1,0,1]
	v_pk_fma_f32 v[132:133], v[132:133], v[36:37], v[62:63] op_sel_hi:[1,0,1]
	s_waitcnt lgkmcnt(2)
	v_pk_fma_f32 v[64:65], v[134:135], v[36:37], v[130:131] op_sel:[0,1,0]
	v_pk_fma_f32 v[62:63], v[136:137], v[36:37], v[132:133] op_sel:[0,1,0]
	ds_read_b128 v[130:133], v129 offset:49152
	ds_read_b128 v[134:137], v129 offset:53248
	s_waitcnt lgkmcnt(3)
; #define LAS __attribute__((address_space(3)))
; __device__ __forceinline__ unsigned cvt_pk_bf16(float lo, float hi) { const f32x2 v = {lo, hi}; const bf16x2_t b = __builtin_convertvector(v, bf16x2_t); return __builtin_bit_cast(unsigned, b); }
; #define H_MLOAD(dst, jj) do { dst[0] = *(const f32x4*)(gp + (jj) * 512); dst[1] = *(const f32x4*)(gp + (jj) * 512 + 4); dst[2] = *(const f32x4*)(m + 4 * DM + (jj) * 512); dst[3] = *(const f32x4*)(m + 4 * DM + (jj) * 512 + 4); \
;             dst[4] = *(const f32x4*)(m + 3 * DM + (jj) * 512); dst[5] = *(const f32x4*)(m + 3 * DM + (jj) * 512 + 4); } while (0)
; __device__ __forceinline__ void ph_norm2_router(const Params& p, int l, LAS unsigned char* lds) {
;     ...
;         for (int j = 0; j < 4; ++j) {
;             if (j < 3) H_MLOAD(mv[(j + 1) & 1], j + 1);
;             const f32x4 ga = mv[j & 1][0], gb = mv[j & 1][1], sa = mv[j & 1][2], sb = mv[j & 1][3], ha = mv[j & 1][4], hb = mv[j & 1][5];
;             float y[8];
; #pragma unroll
;             for (int i = 0; i < 8; ++i) y[i] = x[j][i] * rinv * (i < 4 ? ga[i] : gb[i - 4]) * (1.0f + (i < 4 ? sa[i] : sb[i - 4])) + (i < 4 ? ha[i] : hb[i - 4]);
;             u32x4 h; h.x = cvt_pk_bf16(y[0], y[1]); h.y = cvt_pk_bf16(y[2], y[3]); h.z = cvt_pk_bf16(y[4], y[5]); h.w = cvt_pk_bf16(y[6], y[7]);
;             *(u32x4*)(orow + j * 512) = h;
; #pragma unroll
;             for (int i2 = 0; i2 < 8; i2 += 2) {
; #pragma unroll
;                 for (int e4 = 0; e4 < 4; ++e4) { const f32x4 w0 = *(const LAS f32x4*)(lds + (size_t)(((e4 * 8 + i2) * 256 + j * 64 + lane) * 16)); const f32x4 w1 = *(const LAS f32x4*)(lds + (size_t)(((e4 * 8 + i2 + 1) * 256 + j * 64 + lane) * 16));
;                     lg[e4] = __builtin_elementwise_fma(w0, (f32x4){y[i2], y[i2], y[i2], y[i2]}, lg[e4]); lg[e4] = __builtin_elementwise_fma(w1, (f32x4){y[i2 + 1], y[i2 + 1], y[i2 + 1], y[i2 + 1]}, lg[e4]); }
;                 __builtin_amdgcn_sched_barrier(0); } }
	v_pk_fma_f32 v[42:43], v[42:43], v[36:37], v[196:197] op_sel_hi:[1,0,1]
	v_pk_fma_f32 v[44:45], v[44:45], v[36:37], v[194:195] op_sel_hi:[1,0,1]
	s_waitcnt lgkmcnt(2)
	v_pk_fma_f32 v[196:197], v[46:47], v[36:37], v[42:43] op_sel:[0,1,0]
	v_pk_fma_f32 v[194:195], v[48:49], v[36:37], v[44:45] op_sel:[0,1,0]
	ds_read_b128 v[42:45], v128 offset:24576
	ds_read_b128 v[46:49], v128 offset:28672
	s_waitcnt lgkmcnt(3)
	v_pk_fma_f32 v[130:131], v[130:131], v[36:37], v[56:57] op_sel_hi:[1,0,1]
	v_pk_fma_f32 v[132:133], v[132:133], v[36:37], v[54:55] op_sel_hi:[1,0,1]
	s_waitcnt lgkmcnt(2)
	v_pk_fma_f32 v[54:55], v[136:137], v[36:37], v[132:133] op_sel:[0,1,0]
	v_pk_fma_f32 v[36:37], v[134:135], v[36:37], v[130:131] op_sel:[0,1,0]
	ds_read_b128 v[130:133], v128 offset:57344
	ds_read_b128 v[134:137], v128 offset:61440
	s_waitcnt lgkmcnt(3)
	v_pk_fma_f32 v[42:43], v[42:43], v[34:35], v[60:61] op_sel_hi:[1,0,1]
	v_pk_fma_f32 v[44:45], v[44:45], v[34:35], v[58:59] op_sel_hi:[1,0,1]
	s_waitcnt lgkmcnt(2)
	v_pk_fma_f32 v[200:201], v[46:47], v[34:35], v[42:43] op_sel:[0,1,0]
	v_pk_fma_f32 v[198:199], v[48:49], v[34:35], v[44:45] op_sel:[0,1,0]
	ds_read_b128 v[42:45], v129 offset:24576
	ds_read_b128 v[46:49], v129 offset:28672
	s_waitcnt lgkmcnt(3)
	v_pk_fma_f32 v[130:131], v[130:131], v[34:35], v[64:65] op_sel_hi:[1,0,1]
	v_pk_fma_f32 v[132:133], v[132:133], v[34:35], v[62:63] op_sel_hi:[1,0,1]
	s_waitcnt lgkmcnt(2)
	v_pk_fma_f32 v[204:205], v[134:135], v[34:35], v[130:131] op_sel:[0,1,0]
	v_pk_fma_f32 v[202:203], v[136:137], v[34:35], v[132:133] op_sel:[0,1,0]
	ds_read_b128 v[130:133], v129 offset:57344
	ds_read_b128 v[134:137], v129 offset:61440
	s_waitcnt lgkmcnt(3)
	v_pk_fma_f32 v[42:43], v[42:43], v[34:35], v[196:197] op_sel_hi:[1,0,1]
	v_pk_fma_f32 v[44:45], v[44:45], v[34:35], v[194:195] op_sel_hi:[1,0,1]
	s_waitcnt lgkmcnt(2)
	v_pk_fma_f32 v[196:197], v[46:47], v[34:35], v[42:43] op_sel:[0,1,0]
	v_pk_fma_f32 v[194:195], v[48:49], v[34:35], v[44:45] op_sel:[0,1,0]
	s_waitcnt lgkmcnt(1)
	v_pk_fma_f32 v[36:37], v[130:131], v[34:35], v[36:37] op_sel_hi:[1,0,1]
	v_pk_fma_f32 v[130:131], v[132:133], v[34:35], v[54:55] op_sel_hi:[1,0,1]
	s_waitcnt lgkmcnt(0)
	v_pk_fma_f32 v[210:211], v[134:135], v[34:35], v[36:37] op_sel:[0,1,0]
	v_pk_fma_f32 v[208:209], v[136:137], v[34:35], v[130:131] op_sel:[0,1,0]
	global_load_dwordx4 v[34:37], v[76:77], off offset:16
	global_load_dwordx4 v[62:65], v[76:77], off
	global_load_dwordx4 v[58:61], v[94:95], off
	global_load_dwordx4 v[54:57], v[96:97], off
	global_load_dwordx4 v[42:45], v[38:39], off offset:16
	s_nop 0
	global_load_dwordx4 v[38:41], v[40:41], off offset:16
	v_pk_mul_f32 v[46:47], v[92:93], v[112:113] op_sel_hi:[0,1]
	v_pk_mul_f32 v[22:23], v[22:23], v[46:47]
	ds_read_b128 v[46:49], v128 offset:5120
	v_pk_fma_f32 v[112:113], v[22:23], v[118:119], v[30:31]
	v_pk_mul_f32 v[22:23], v[92:93], v[110:111] op_sel_hi:[0,1]
	v_pk_mul_f32 v[22:23], v[24:25], v[22:23]
	v_cvt_pk_bf16_f32 v24, v112, v113
	v_pk_fma_f32 v[32:33], v[22:23], v[116:117], v[32:33]
	v_pk_mul_f32 v[22:23], v[92:93], v[52:53] op_sel_hi:[0,1]
	v_pk_mul_f32 v[18:19], v[18:19], v[22:23]
	v_cvt_pk_bf16_f32 v25, v32, v33
	s_waitcnt vmcnt(7)
	v_pk_fma_f32 v[22:23], v[18:19], v[114:115], v[26:27]
	v_pk_mul_f32 v[18:19], v[92:93], v[50:51] op_sel_hi:[0,1]
	v_pk_mul_f32 v[18:19], v[20:21], v[18:19]
	v_cvt_pk_bf16_f32 v26, v22, v23
	v_pk_fma_f32 v[18:19], v[18:19], v[120:121], v[28:29]
	ds_read_b128 v[28:31], v128 offset:1024
	v_cvt_pk_bf16_f32 v27, v18, v19
	global_store_dwordx4 v[90:91], v[24:27], off offset:1024
	ds_read_b128 v[24:27], v128 offset:33792
	s_waitcnt lgkmcnt(1)
	v_pk_fma_f32 v[20:21], v[28:29], v[112:113], v[200:201] op_sel_hi:[1,0,1]
	v_pk_fma_f32 v[28:29], v[30:31], v[112:113], v[198:199] op_sel_hi:[1,0,1]
	v_pk_fma_f32 v[20:21], v[46:47], v[112:113], v[20:21] op_sel:[0,1,0]
	v_pk_fma_f32 v[50:51], v[48:49], v[112:113], v[28:29] op_sel:[0,1,0]
	ds_read_b128 v[28:31], v128 offset:37888
	ds_read_b128 v[46:49], v129 offset:1024
	s_waitcnt lgkmcnt(2)
	v_pk_fma_f32 v[24:25], v[24:25], v[112:113], v[204:205] op_sel_hi:[1,0,1]
	v_pk_fma_f32 v[26:27], v[26:27], v[112:113], v[202:203] op_sel_hi:[1,0,1]
	s_waitcnt lgkmcnt(1)
	v_pk_fma_f32 v[110:111], v[28:29], v[112:113], v[24:25] op_sel:[0,1,0]
	v_pk_fma_f32 v[52:53], v[30:31], v[112:113], v[26:27] op_sel:[0,1,0]
	ds_read_b128 v[24:27], v129 offset:5120
	ds_read_b128 v[28:31], v129 offset:33792
	s_waitcnt lgkmcnt(2)
	v_pk_fma_f32 v[114:115], v[46:47], v[112:113], v[196:197] op_sel_hi:[1,0,1]
	v_pk_fma_f32 v[116:117], v[48:49], v[112:113], v[194:195] op_sel_hi:[1,0,1]
	ds_read_b128 v[46:49], v129 offset:37888
	s_waitcnt lgkmcnt(2)
	v_pk_fma_f32 v[116:117], v[26:27], v[112:113], v[116:117] op_sel:[0,1,0]
	v_pk_fma_f32 v[114:115], v[24:25], v[112:113], v[114:115] op_sel:[0,1,0]
	s_waitcnt lgkmcnt(1)
	v_pk_fma_f32 v[24:25], v[28:29], v[112:113], v[210:211] op_sel_hi:[1,0,1]
	v_pk_fma_f32 v[26:27], v[30:31], v[112:113], v[208:209] op_sel_hi:[1,0,1]
	s_waitcnt lgkmcnt(0)
	v_pk_fma_f32 v[46:47], v[46:47], v[112:113], v[24:25] op_sel:[0,1,0]
	v_pk_fma_f32 v[48:49], v[48:49], v[112:113], v[26:27] op_sel:[0,1,0]
	ds_read_b128 v[24:27], v128 offset:9216
	ds_read_b128 v[28:31], v128 offset:13312
	ds_read_b128 v[130:133], v128 offset:41984
	ds_read_b128 v[134:137], v128 offset:46080
	s_waitcnt lgkmcnt(3)
	v_pk_fma_f32 v[20:21], v[24:25], v[32:33], v[20:21] op_sel_hi:[1,0,1]
	v_pk_fma_f32 v[24:25], v[26:27], v[32:33], v[50:51] op_sel_hi:[1,0,1]
	s_waitcnt lgkmcnt(2)
	v_pk_fma_f32 v[20:21], v[28:29], v[32:33], v[20:21] op_sel:[0,1,0]
	v_pk_fma_f32 v[50:51], v[30:31], v[32:33], v[24:25] op_sel:[0,1,0]
	ds_read_b128 v[24:27], v129 offset:9216
	ds_read_b128 v[28:31], v129 offset:13312
	s_waitcnt lgkmcnt(3)
; #define LAS __attribute__((address_space(3)))
; __device__ __forceinline__ unsigned cvt_pk_bf16(float lo, float hi) { const f32x2 v = {lo, hi}; const bf16x2_t b = __builtin_convertvector(v, bf16x2_t); return __builtin_bit_cast(unsigned, b); }
; #define H_MLOAD(dst, jj) do { dst[0] = *(const f32x4*)(gp + (jj) * 512); dst[1] = *(const f32x4*)(gp + (jj) * 512 + 4); dst[2] = *(const f32x4*)(m + 4 * DM + (jj) * 512); dst[3] = *(const f32x4*)(m + 4 * DM + (jj) * 512 + 4); \
;             dst[4] = *(const f32x4*)(m + 3 * DM + (jj) * 512); dst[5] = *(const f32x4*)(m + 3 * DM + (jj) * 512 + 4); } while (0)
; __device__ __forceinline__ void ph_norm2_router(const Params& p, int l, LAS unsigned char* lds) {
;     ...
;         for (int j = 0; j < 4; ++j) {
;             if (j < 3) H_MLOAD(mv[(j + 1) & 1], j + 1);
;             const f32x4 ga = mv[j & 1][0], gb = mv[j & 1][1], sa = mv[j & 1][2], sb = mv[j & 1][3], ha = mv[j & 1][4], hb = mv[j & 1][5];
;             float y[8];
; #pragma unroll
;             for (int i = 0; i < 8; ++i) y[i] = x[j][i] * rinv * (i < 4 ? ga[i] : gb[i - 4]) * (1.0f + (i < 4 ? sa[i] : sb[i - 4])) + (i < 4 ? ha[i] : hb[i - 4]);
;             u32x4 h; h.x = cvt_pk_bf16(y[0], y[1]); h.y = cvt_pk_bf16(y[2], y[3]); h.z = cvt_pk_bf16(y[4], y[5]); h.w = cvt_pk_bf16(y[6], y[7]);
;             *(u32x4*)(orow + j * 512) = h;
; #pragma unroll
;             for (int i2 = 0; i2 < 8; i2 += 2) {
; #pragma unroll
;                 for (int e4 = 0; e4 < 4; ++e4) { const f32x4 w0 = *(const LAS f32x4*)(lds + (size_t)(((e4 * 8 + i2) * 256 + j * 64 + lane) * 16)); const f32x4 w1 = *(const LAS f32x4*)(lds + (size_t)(((e4 * 8 + i2 + 1) * 256 + j * 64 + lane) * 16));
;                     lg[e4] = __builtin_elementwise_fma(w0, (f32x4){y[i2], y[i2], y[i2], y[i2]}, lg[e4]); lg[e4] = __builtin_elementwise_fma(w1, (f32x4){y[i2 + 1], y[i2 + 1], y[i2 + 1], y[i2 + 1]}, lg[e4]); }
;                 __builtin_amdgcn_sched_barrier(0); } }
	v_pk_fma_f32 v[130:131], v[130:131], v[32:33], v[110:111] op_sel_hi:[1,0,1]
	v_pk_fma_f32 v[132:133], v[132:133], v[32:33], v[52:53] op_sel_hi:[1,0,1]
	s_waitcnt lgkmcnt(2)
	v_pk_fma_f32 v[110:111], v[134:135], v[32:33], v[130:131] op_sel:[0,1,0]
	v_pk_fma_f32 v[52:53], v[136:137], v[32:33], v[132:133] op_sel:[0,1,0]
	ds_read_b128 v[130:133], v129 offset:41984
	ds_read_b128 v[134:137], v129 offset:46080
	s_waitcnt lgkmcnt(3)
	v_pk_fma_f32 v[24:25], v[24:25], v[32:33], v[114:115] op_sel_hi:[1,0,1]
	v_pk_fma_f32 v[26:27], v[26:27], v[32:33], v[116:117] op_sel_hi:[1,0,1]
	s_waitcnt lgkmcnt(2)
	v_pk_fma_f32 v[114:115], v[28:29], v[32:33], v[24:25] op_sel:[0,1,0]
	v_pk_fma_f32 v[112:113], v[30:31], v[32:33], v[26:27] op_sel:[0,1,0]
	ds_read_b128 v[24:27], v128 offset:17408
	ds_read_b128 v[28:31], v128 offset:21504
	s_waitcnt lgkmcnt(3)
	v_pk_fma_f32 v[130:131], v[130:131], v[32:33], v[46:47] op_sel_hi:[1,0,1]
	v_pk_fma_f32 v[132:133], v[132:133], v[32:33], v[48:49] op_sel_hi:[1,0,1]
	s_waitcnt lgkmcnt(2)
	v_pk_fma_f32 v[46:47], v[136:137], v[32:33], v[132:133] op_sel:[0,1,0]
	v_pk_fma_f32 v[32:33], v[134:135], v[32:33], v[130:131] op_sel:[0,1,0]
	ds_read_b128 v[130:133], v128 offset:50176
	ds_read_b128 v[134:137], v128 offset:54272
	s_waitcnt lgkmcnt(3)
	v_pk_fma_f32 v[20:21], v[24:25], v[22:23], v[20:21] op_sel_hi:[1,0,1]
	v_pk_fma_f32 v[24:25], v[26:27], v[22:23], v[50:51] op_sel_hi:[1,0,1]
	s_waitcnt lgkmcnt(2)
	v_pk_fma_f32 v[50:51], v[28:29], v[22:23], v[20:21] op_sel:[0,1,0]
	v_pk_fma_f32 v[48:49], v[30:31], v[22:23], v[24:25] op_sel:[0,1,0]
	ds_read_b128 v[24:27], v129 offset:17408
	ds_read_b128 v[28:31], v129 offset:21504
	s_waitcnt lgkmcnt(3)
	v_pk_fma_f32 v[20:21], v[130:131], v[22:23], v[110:111] op_sel_hi:[1,0,1]
	v_pk_fma_f32 v[130:131], v[132:133], v[22:23], v[52:53] op_sel_hi:[1,0,1]
	s_waitcnt lgkmcnt(2)
	v_pk_fma_f32 v[110:111], v[134:135], v[22:23], v[20:21] op_sel:[0,1,0]
	v_pk_fma_f32 v[52:53], v[136:137], v[22:23], v[130:131] op_sel:[0,1,0]
	s_waitcnt lgkmcnt(1)
	v_pk_fma_f32 v[20:21], v[24:25], v[22:23], v[114:115] op_sel_hi:[1,0,1]
	v_pk_fma_f32 v[24:25], v[26:27], v[22:23], v[112:113] op_sel_hi:[1,0,1]
	s_waitcnt lgkmcnt(0)
	v_pk_fma_f32 v[114:115], v[28:29], v[22:23], v[20:21] op_sel:[0,1,0]
	v_pk_fma_f32 v[112:113], v[30:31], v[22:23], v[24:25] op_sel:[0,1,0]
	ds_read_b128 v[24:27], v129 offset:50176
	ds_read_b128 v[28:31], v129 offset:54272
	ds_read_b128 v[130:133], v128 offset:25600
	ds_read_b128 v[134:137], v128 offset:29696
	s_waitcnt lgkmcnt(3)
	v_pk_fma_f32 v[20:21], v[24:25], v[22:23], v[32:33] op_sel_hi:[1,0,1]
	v_pk_fma_f32 v[24:25], v[26:27], v[22:23], v[46:47] op_sel_hi:[1,0,1]
	s_waitcnt lgkmcnt(2)
	v_pk_fma_f32 v[28:29], v[28:29], v[22:23], v[20:21] op_sel:[0,1,0]
	v_pk_fma_f32 v[30:31], v[30:31], v[22:23], v[24:25] op_sel:[0,1,0]
	ds_read_b128 v[20:23], v128 offset:58368
	ds_read_b128 v[24:27], v128 offset:62464
	s_waitcnt lgkmcnt(3)
	v_pk_fma_f32 v[130:131], v[130:131], v[18:19], v[50:51] op_sel_hi:[1,0,1]
	v_pk_fma_f32 v[132:133], v[132:133], v[18:19], v[48:49] op_sel_hi:[1,0,1]
	s_waitcnt lgkmcnt(2)
	v_pk_fma_f32 v[118:119], v[134:135], v[18:19], v[130:131] op_sel:[0,1,0]
	v_pk_fma_f32 v[116:117], v[136:137], v[18:19], v[132:133] op_sel:[0,1,0]
	ds_read_b128 v[130:133], v129 offset:25600
	ds_read_b128 v[134:137], v129 offset:29696
	s_waitcnt lgkmcnt(3)
	v_pk_fma_f32 v[20:21], v[20:21], v[18:19], v[110:111] op_sel_hi:[1,0,1]
	v_pk_fma_f32 v[22:23], v[22:23], v[18:19], v[52:53] op_sel_hi:[1,0,1]
	s_waitcnt lgkmcnt(2)
	v_pk_fma_f32 v[120:121], v[24:25], v[18:19], v[20:21] op_sel:[0,1,0]
	v_pk_fma_f32 v[110:111], v[26:27], v[18:19], v[22:23] op_sel:[0,1,0]
	ds_read_b128 v[20:23], v129 offset:58368
	ds_read_b128 v[24:27], v129 offset:62464
	s_waitcnt lgkmcnt(3)
	v_pk_fma_f32 v[130:131], v[130:131], v[18:19], v[114:115] op_sel_hi:[1,0,1]
	v_pk_fma_f32 v[132:133], v[132:133], v[18:19], v[112:113] op_sel_hi:[1,0,1]
	s_waitcnt lgkmcnt(2)
	v_pk_fma_f32 v[114:115], v[134:135], v[18:19], v[130:131] op_sel:[0,1,0]
	v_pk_fma_f32 v[112:113], v[136:137], v[18:19], v[132:133] op_sel:[0,1,0]
	s_waitcnt lgkmcnt(1)
	v_pk_fma_f32 v[20:21], v[20:21], v[18:19], v[28:29] op_sel_hi:[1,0,1]
	v_pk_fma_f32 v[22:23], v[22:23], v[18:19], v[30:31] op_sel_hi:[1,0,1]
	s_waitcnt lgkmcnt(0)
	v_pk_fma_f32 v[196:197], v[24:25], v[18:19], v[20:21] op_sel:[0,1,0]
	v_pk_fma_f32 v[194:195], v[26:27], v[18:19], v[22:23] op_sel:[0,1,0]
	global_load_dwordx4 v[18:21], v[78:79], off offset:16
	global_load_dwordx4 v[50:53], v[78:79], off
	global_load_dwordx4 v[46:49], v[94:95], off offset:2048
	global_load_dwordx4 v[30:33], v[96:97], off offset:2048
	global_load_dwordx4 v[26:29], v[106:107], off offset:16
	global_load_dwordx4 v[22:25], v[108:109], off offset:16
	v_pk_mul_f32 v[94:95], v[92:93], v[104:105] op_sel_hi:[0,1]
	s_waitcnt vmcnt(11)
	v_pk_mul_f32 v[62:63], v[94:95], v[62:63]
	s_waitcnt vmcnt(10)
	v_pk_add_f32 v[58:59], v[58:59], 1.0 op_sel_hi:[1,0]
	s_waitcnt vmcnt(8)
	v_pk_add_f32 v[42:43], v[42:43], 1.0 op_sel_hi:[1,0]
	v_pk_fma_f32 v[62:63], v[62:63], v[58:59], v[54:55]
	v_pk_mul_f32 v[54:55], v[92:93], v[102:103] op_sel_hi:[0,1]
	v_pk_mul_f32 v[54:55], v[54:55], v[64:65]
	v_pk_add_f32 v[58:59], v[60:61], 1.0 op_sel_hi:[1,0]
	s_nop 0
	v_pk_fma_f32 v[64:65], v[54:55], v[58:59], v[56:57]
	v_pk_mul_f32 v[54:55], v[92:93], v[100:101] op_sel_hi:[0,1]
	v_pk_mul_f32 v[34:35], v[54:55], v[34:35]
	ds_read_b128 v[54:57], v128 offset:2048
	ds_read_b128 v[58:61], v128 offset:6144
	s_waitcnt vmcnt(7)
; #define LAS __attribute__((address_space(3)))
; __device__ __forceinline__ unsigned cvt_pk_bf16(float lo, float hi) { const f32x2 v = {lo, hi}; const bf16x2_t b = __builtin_convertvector(v, bf16x2_t); return __builtin_bit_cast(unsigned, b); }
; #define H_MLOAD(dst, jj) do { dst[0] = *(const f32x4*)(gp + (jj) * 512); dst[1] = *(const f32x4*)(gp + (jj) * 512 + 4); dst[2] = *(const f32x4*)(m + 4 * DM + (jj) * 512); dst[3] = *(const f32x4*)(m + 4 * DM + (jj) * 512 + 4); \
;             dst[4] = *(const f32x4*)(m + 3 * DM + (jj) * 512); dst[5] = *(const f32x4*)(m + 3 * DM + (jj) * 512 + 4); } while (0)
; __device__ __forceinline__ void ph_norm2_router(const Params& p, int l, LAS unsigned char* lds) {
;     ...
;         for (int j = 0; j < 4; ++j) {
;             if (j < 3) H_MLOAD(mv[(j + 1) & 1], j + 1);
;             const f32x4 ga = mv[j & 1][0], gb = mv[j & 1][1], sa = mv[j & 1][2], sb = mv[j & 1][3], ha = mv[j & 1][4], hb = mv[j & 1][5];
;             float y[8];
; #pragma unroll
;             for (int i = 0; i < 8; ++i) y[i] = x[j][i] * rinv * (i < 4 ? ga[i] : gb[i - 4]) * (1.0f + (i < 4 ? sa[i] : sb[i - 4])) + (i < 4 ? ha[i] : hb[i - 4]);
;             u32x4 h; h.x = cvt_pk_bf16(y[0], y[1]); h.y = cvt_pk_bf16(y[2], y[3]); h.z = cvt_pk_bf16(y[4], y[5]); h.w = cvt_pk_bf16(y[6], y[7]);
;             *(u32x4*)(orow + j * 512) = h;
; #pragma unroll
;             for (int i2 = 0; i2 < 8; i2 += 2) {
; #pragma unroll
;                 for (int e4 = 0; e4 < 4; ++e4) { const f32x4 w0 = *(const LAS f32x4*)(lds + (size_t)(((e4 * 8 + i2) * 256 + j * 64 + lane) * 16)); const f32x4 w1 = *(const LAS f32x4*)(lds + (size_t)(((e4 * 8 + i2 + 1) * 256 + j * 64 + lane) * 16));
;                     lg[e4] = __builtin_elementwise_fma(w0, (f32x4){y[i2], y[i2], y[i2], y[i2]}, lg[e4]); lg[e4] = __builtin_elementwise_fma(w1, (f32x4){y[i2 + 1], y[i2 + 1], y[i2 + 1], y[i2 + 1]}, lg[e4]); }
;                 __builtin_amdgcn_sched_barrier(0); } }
	v_pk_fma_f32 v[38:39], v[34:35], v[42:43], v[38:39]
	v_pk_mul_f32 v[34:35], v[92:93], v[98:99] op_sel_hi:[0,1]
	v_pk_mul_f32 v[34:35], v[34:35], v[36:37]
	v_pk_add_f32 v[36:37], v[44:45], 1.0 op_sel_hi:[1,0]
	v_cvt_pk_bf16_f32 v42, v38, v39
	v_pk_fma_f32 v[34:35], v[34:35], v[36:37], v[40:41]
	v_cvt_pk_bf16_f32 v40, v62, v63
	v_cvt_pk_bf16_f32 v41, v64, v65
	v_cvt_pk_bf16_f32 v43, v34, v35
	global_store_dwordx4 v[90:91], v[40:43], off offset:2048
	ds_read_b128 v[40:43], v128 offset:34816
	s_waitcnt lgkmcnt(2)
	v_pk_fma_f32 v[36:37], v[54:55], v[62:63], v[118:119] op_sel_hi:[1,0,1]
	v_pk_fma_f32 v[44:45], v[56:57], v[62:63], v[116:117] op_sel_hi:[1,0,1]
	ds_read_b128 v[54:57], v128 offset:38912
	s_waitcnt lgkmcnt(2)
	v_pk_fma_f32 v[44:45], v[60:61], v[62:63], v[44:45] op_sel:[0,1,0]
	v_pk_fma_f32 v[36:37], v[58:59], v[62:63], v[36:37] op_sel:[0,1,0]
	ds_read_b128 v[58:61], v129 offset:2048
	s_waitcnt lgkmcnt(2)
	v_pk_fma_f32 v[40:41], v[40:41], v[62:63], v[120:121] op_sel_hi:[1,0,1]
	v_pk_fma_f32 v[42:43], v[42:43], v[62:63], v[110:111] op_sel_hi:[1,0,1]
	s_waitcnt lgkmcnt(1)
	v_pk_fma_f32 v[96:97], v[54:55], v[62:63], v[40:41] op_sel:[0,1,0]
	v_pk_fma_f32 v[94:95], v[56:57], v[62:63], v[42:43] op_sel:[0,1,0]
	ds_read_b128 v[40:43], v129 offset:6144
	ds_read_b128 v[54:57], v129 offset:34816
	s_waitcnt lgkmcnt(2)
	v_pk_fma_f32 v[98:99], v[58:59], v[62:63], v[114:115] op_sel_hi:[1,0,1]
	v_pk_fma_f32 v[100:101], v[60:61], v[62:63], v[112:113] op_sel_hi:[1,0,1]
	ds_read_b128 v[58:61], v129 offset:38912
	s_waitcnt lgkmcnt(2)
	v_pk_fma_f32 v[100:101], v[42:43], v[62:63], v[100:101] op_sel:[0,1,0]
	v_pk_fma_f32 v[98:99], v[40:41], v[62:63], v[98:99] op_sel:[0,1,0]
	s_waitcnt lgkmcnt(1)
	v_pk_fma_f32 v[40:41], v[54:55], v[62:63], v[196:197] op_sel_hi:[1,0,1]
	v_pk_fma_f32 v[42:43], v[56:57], v[62:63], v[194:195] op_sel_hi:[1,0,1]
	s_waitcnt lgkmcnt(0)
	v_pk_fma_f32 v[58:59], v[58:59], v[62:63], v[40:41] op_sel:[0,1,0]
	v_pk_fma_f32 v[60:61], v[60:61], v[62:63], v[42:43] op_sel:[0,1,0]
	ds_read_b128 v[40:43], v128 offset:10240
	ds_read_b128 v[54:57], v128 offset:14336
	ds_read_b128 v[130:133], v128 offset:43008
	ds_read_b128 v[134:137], v128 offset:47104
	s_waitcnt lgkmcnt(3)
	v_pk_fma_f32 v[36:37], v[40:41], v[64:65], v[36:37] op_sel_hi:[1,0,1]
	v_pk_fma_f32 v[40:41], v[42:43], v[64:65], v[44:45] op_sel_hi:[1,0,1]
	s_waitcnt lgkmcnt(2)
	v_pk_fma_f32 v[36:37], v[54:55], v[64:65], v[36:37] op_sel:[0,1,0]
	v_pk_fma_f32 v[44:45], v[56:57], v[64:65], v[40:41] op_sel:[0,1,0]
	ds_read_b128 v[40:43], v129 offset:10240
	ds_read_b128 v[54:57], v129 offset:14336
	s_waitcnt lgkmcnt(3)
	v_pk_fma_f32 v[130:131], v[130:131], v[64:65], v[96:97] op_sel_hi:[1,0,1]
	v_pk_fma_f32 v[132:133], v[132:133], v[64:65], v[94:95] op_sel_hi:[1,0,1]
	s_waitcnt lgkmcnt(2)
	v_pk_fma_f32 v[94:95], v[134:135], v[64:65], v[130:131] op_sel:[0,1,0]
	v_pk_fma_f32 v[62:63], v[136:137], v[64:65], v[132:133] op_sel:[0,1,0]
	ds_read_b128 v[130:133], v129 offset:43008
	ds_read_b128 v[134:137], v129 offset:47104
	s_waitcnt lgkmcnt(3)
	v_pk_fma_f32 v[40:41], v[40:41], v[64:65], v[98:99] op_sel_hi:[1,0,1]
	v_pk_fma_f32 v[42:43], v[42:43], v[64:65], v[100:101] op_sel_hi:[1,0,1]
	s_waitcnt lgkmcnt(2)
	v_pk_fma_f32 v[98:99], v[54:55], v[64:65], v[40:41] op_sel:[0,1,0]
	v_pk_fma_f32 v[96:97], v[56:57], v[64:65], v[42:43] op_sel:[0,1,0]
	ds_read_b128 v[40:43], v128 offset:18432
	ds_read_b128 v[54:57], v128 offset:22528
	s_waitcnt lgkmcnt(3)
	v_pk_fma_f32 v[130:131], v[130:131], v[64:65], v[58:59] op_sel_hi:[1,0,1]
	v_pk_fma_f32 v[132:133], v[132:133], v[64:65], v[60:61] op_sel_hi:[1,0,1]
	s_waitcnt lgkmcnt(2)
	v_pk_fma_f32 v[60:61], v[134:135], v[64:65], v[130:131] op_sel:[0,1,0]
	v_pk_fma_f32 v[58:59], v[136:137], v[64:65], v[132:133] op_sel:[0,1,0]
	ds_read_b128 v[130:133], v128 offset:51200
	ds_read_b128 v[134:137], v128 offset:55296
	s_waitcnt lgkmcnt(3)
	v_pk_fma_f32 v[36:37], v[40:41], v[38:39], v[36:37] op_sel_hi:[1,0,1]
	v_pk_fma_f32 v[40:41], v[42:43], v[38:39], v[44:45] op_sel_hi:[1,0,1]
	s_waitcnt lgkmcnt(2)
	v_pk_fma_f32 v[64:65], v[54:55], v[38:39], v[36:37] op_sel:[0,1,0]
	v_pk_fma_f32 v[44:45], v[56:57], v[38:39], v[40:41] op_sel:[0,1,0]
	ds_read_b128 v[40:43], v129 offset:18432
	ds_read_b128 v[54:57], v129 offset:22528
	s_waitcnt lgkmcnt(3)
	v_pk_fma_f32 v[36:37], v[130:131], v[38:39], v[94:95] op_sel_hi:[1,0,1]
	v_pk_fma_f32 v[130:131], v[132:133], v[38:39], v[62:63] op_sel_hi:[1,0,1]
	s_waitcnt lgkmcnt(2)
	v_pk_fma_f32 v[94:95], v[134:135], v[38:39], v[36:37] op_sel:[0,1,0]
	v_pk_fma_f32 v[62:63], v[136:137], v[38:39], v[130:131] op_sel:[0,1,0]
	s_waitcnt lgkmcnt(1)
	v_pk_fma_f32 v[36:37], v[40:41], v[38:39], v[98:99] op_sel_hi:[1,0,1]
	v_pk_fma_f32 v[40:41], v[42:43], v[38:39], v[96:97] op_sel_hi:[1,0,1]
	s_waitcnt lgkmcnt(0)
	v_pk_fma_f32 v[98:99], v[54:55], v[38:39], v[36:37] op_sel:[0,1,0]
	v_pk_fma_f32 v[96:97], v[56:57], v[38:39], v[40:41] op_sel:[0,1,0]
	ds_read_b128 v[40:43], v129 offset:51200
	ds_read_b128 v[54:57], v129 offset:55296
	ds_read_b128 v[130:133], v128 offset:26624
	ds_read_b128 v[134:137], v128 offset:30720
	s_waitcnt lgkmcnt(3)
	v_pk_fma_f32 v[36:37], v[40:41], v[38:39], v[60:61] op_sel_hi:[1,0,1]
	v_pk_fma_f32 v[40:41], v[42:43], v[38:39], v[58:59] op_sel_hi:[1,0,1]
	s_waitcnt lgkmcnt(2)
	v_pk_fma_f32 v[54:55], v[54:55], v[38:39], v[36:37] op_sel:[0,1,0]
	v_pk_fma_f32 v[56:57], v[56:57], v[38:39], v[40:41] op_sel:[0,1,0]
	ds_read_b128 v[36:39], v128 offset:59392
	ds_read_b128 v[40:43], v128 offset:63488
	s_waitcnt lgkmcnt(3)
	v_pk_fma_f32 v[130:131], v[130:131], v[34:35], v[64:65] op_sel_hi:[1,0,1]
	v_pk_fma_f32 v[132:133], v[132:133], v[34:35], v[44:45] op_sel_hi:[1,0,1]
	s_waitcnt lgkmcnt(2)
; #define LAS __attribute__((address_space(3)))
; __device__ __forceinline__ unsigned cvt_pk_bf16(float lo, float hi) { const f32x2 v = {lo, hi}; const bf16x2_t b = __builtin_convertvector(v, bf16x2_t); return __builtin_bit_cast(unsigned, b); }
; #define H_MLOAD(dst, jj) do { dst[0] = *(const f32x4*)(gp + (jj) * 512); dst[1] = *(const f32x4*)(gp + (jj) * 512 + 4); dst[2] = *(const f32x4*)(m + 4 * DM + (jj) * 512); dst[3] = *(const f32x4*)(m + 4 * DM + (jj) * 512 + 4); \
;             dst[4] = *(const f32x4*)(m + 3 * DM + (jj) * 512); dst[5] = *(const f32x4*)(m + 3 * DM + (jj) * 512 + 4); } while (0)
; __device__ __forceinline__ void ph_norm2_router(const Params& p, int l, LAS unsigned char* lds) {
;     ...
;         for (int j = 0; j < 4; ++j) {
;             if (j < 3) H_MLOAD(mv[(j + 1) & 1], j + 1);
;             const f32x4 ga = mv[j & 1][0], gb = mv[j & 1][1], sa = mv[j & 1][2], sb = mv[j & 1][3], ha = mv[j & 1][4], hb = mv[j & 1][5];
;             float y[8];
; #pragma unroll
;             for (int i = 0; i < 8; ++i) y[i] = x[j][i] * rinv * (i < 4 ? ga[i] : gb[i - 4]) * (1.0f + (i < 4 ? sa[i] : sb[i - 4])) + (i < 4 ? ha[i] : hb[i - 4]);
;             u32x4 h; h.x = cvt_pk_bf16(y[0], y[1]); h.y = cvt_pk_bf16(y[2], y[3]); h.z = cvt_pk_bf16(y[4], y[5]); h.w = cvt_pk_bf16(y[6], y[7]);
;             *(u32x4*)(orow + j * 512) = h;
; #pragma unroll
;             for (int i2 = 0; i2 < 8; i2 += 2) {
; #pragma unroll
;                 for (int e4 = 0; e4 < 4; ++e4) { const f32x4 w0 = *(const LAS f32x4*)(lds + (size_t)(((e4 * 8 + i2) * 256 + j * 64 + lane) * 16)); const f32x4 w1 = *(const LAS f32x4*)(lds + (size_t)(((e4 * 8 + i2 + 1) * 256 + j * 64 + lane) * 16));
;                     lg[e4] = __builtin_elementwise_fma(w0, (f32x4){y[i2], y[i2], y[i2], y[i2]}, lg[e4]); lg[e4] = __builtin_elementwise_fma(w1, (f32x4){y[i2 + 1], y[i2 + 1], y[i2 + 1], y[i2 + 1]}, lg[e4]); }
;                 __builtin_amdgcn_sched_barrier(0); } }
	v_pk_fma_f32 v[58:59], v[134:135], v[34:35], v[130:131] op_sel:[0,1,0]
	v_pk_fma_f32 v[44:45], v[136:137], v[34:35], v[132:133] op_sel:[0,1,0]
	ds_read_b128 v[130:133], v129 offset:26624
	ds_read_b128 v[134:137], v129 offset:30720
	s_waitcnt lgkmcnt(3)
	v_pk_fma_f32 v[36:37], v[36:37], v[34:35], v[94:95] op_sel_hi:[1,0,1]
	v_pk_fma_f32 v[38:39], v[38:39], v[34:35], v[62:63] op_sel_hi:[1,0,1]
	s_waitcnt lgkmcnt(2)
	v_pk_fma_f32 v[62:63], v[40:41], v[34:35], v[36:37] op_sel:[0,1,0]
	v_pk_fma_f32 v[60:61], v[42:43], v[34:35], v[38:39] op_sel:[0,1,0]
	ds_read_b128 v[36:39], v129 offset:59392
	ds_read_b128 v[40:43], v129 offset:63488
	s_waitcnt lgkmcnt(3)
	v_pk_fma_f32 v[130:131], v[130:131], v[34:35], v[98:99] op_sel_hi:[1,0,1]
	v_pk_fma_f32 v[132:133], v[132:133], v[34:35], v[96:97] op_sel_hi:[1,0,1]
	s_waitcnt lgkmcnt(2)
	v_pk_fma_f32 v[94:95], v[134:135], v[34:35], v[130:131] op_sel:[0,1,0]
	v_pk_fma_f32 v[64:65], v[136:137], v[34:35], v[132:133] op_sel:[0,1,0]
	s_waitcnt lgkmcnt(1)
	v_pk_fma_f32 v[36:37], v[36:37], v[34:35], v[54:55] op_sel_hi:[1,0,1]
	v_pk_fma_f32 v[38:39], v[38:39], v[34:35], v[56:57] op_sel_hi:[1,0,1]
	s_waitcnt lgkmcnt(0)
	v_pk_fma_f32 v[36:37], v[40:41], v[34:35], v[36:37] op_sel:[0,1,0]
	v_pk_fma_f32 v[38:39], v[42:43], v[34:35], v[38:39] op_sel:[0,1,0]
	v_pk_mul_f32 v[34:35], v[92:93], v[88:89] op_sel_hi:[0,1]
	s_waitcnt vmcnt(5)
	v_pk_mul_f32 v[34:35], v[34:35], v[50:51]
	s_waitcnt vmcnt(4)
	v_pk_add_f32 v[40:41], v[46:47], 1.0 op_sel_hi:[1,0]
	s_waitcnt vmcnt(2)
	v_pk_add_f32 v[26:27], v[26:27], 1.0 op_sel_hi:[1,0]
	v_pk_fma_f32 v[40:41], v[34:35], v[40:41], v[30:31]
	v_pk_mul_f32 v[30:31], v[92:93], v[86:87] op_sel_hi:[0,1]
	v_pk_mul_f32 v[30:31], v[30:31], v[52:53]
	v_pk_add_f32 v[34:35], v[48:49], 1.0 op_sel_hi:[1,0]
	s_nop 0
	v_pk_fma_f32 v[42:43], v[30:31], v[34:35], v[32:33]
	v_pk_mul_f32 v[30:31], v[92:93], v[84:85] op_sel_hi:[0,1]
	v_pk_mul_f32 v[18:19], v[30:31], v[18:19]
	ds_read_b128 v[32:35], v128 offset:7168
	s_waitcnt vmcnt(1)
	v_pk_fma_f32 v[22:23], v[18:19], v[26:27], v[22:23]
	v_pk_mul_f32 v[18:19], v[92:93], v[82:83] op_sel_hi:[0,1]
	v_pk_mul_f32 v[18:19], v[18:19], v[20:21]
	v_pk_add_f32 v[20:21], v[28:29], 1.0 op_sel_hi:[1,0]
	ds_read_b128 v[28:31], v128 offset:3072
	v_pk_fma_f32 v[18:19], v[18:19], v[20:21], v[24:25]
	v_cvt_pk_bf16_f32 v24, v40, v41
	v_cvt_pk_bf16_f32 v25, v42, v43
	v_cvt_pk_bf16_f32 v26, v22, v23
	v_cvt_pk_bf16_f32 v27, v18, v19
	global_store_dwordx4 v[90:91], v[24:27], off offset:3072
	s_waitcnt lgkmcnt(0)
	v_pk_fma_f32 v[20:21], v[28:29], v[40:41], v[58:59] op_sel_hi:[1,0,1]
	ds_read_b128 v[24:27], v128 offset:35840
	v_pk_fma_f32 v[28:29], v[30:31], v[40:41], v[44:45] op_sel_hi:[1,0,1]
	v_pk_fma_f32 v[20:21], v[32:33], v[40:41], v[20:21] op_sel:[0,1,0]
	v_pk_fma_f32 v[44:45], v[34:35], v[40:41], v[28:29] op_sel:[0,1,0]
	ds_read_b128 v[28:31], v128 offset:39936
	ds_read_b128 v[32:35], v129 offset:3072
	s_waitcnt lgkmcnt(2)
	v_pk_fma_f32 v[24:25], v[24:25], v[40:41], v[62:63] op_sel_hi:[1,0,1]
	v_pk_fma_f32 v[26:27], v[26:27], v[40:41], v[60:61] op_sel_hi:[1,0,1]
	s_waitcnt lgkmcnt(1)
	v_pk_fma_f32 v[48:49], v[28:29], v[40:41], v[24:25] op_sel:[0,1,0]
	v_pk_fma_f32 v[46:47], v[30:31], v[40:41], v[26:27] op_sel:[0,1,0]
	ds_read_b128 v[24:27], v129 offset:7168
	ds_read_b128 v[28:31], v129 offset:35840
	s_waitcnt lgkmcnt(2)
	v_pk_fma_f32 v[50:51], v[32:33], v[40:41], v[94:95] op_sel_hi:[1,0,1]
	v_pk_fma_f32 v[52:53], v[34:35], v[40:41], v[64:65] op_sel_hi:[1,0,1]
	ds_read_b128 v[32:35], v129 offset:39936
	s_waitcnt lgkmcnt(2)
	v_pk_fma_f32 v[52:53], v[26:27], v[40:41], v[52:53] op_sel:[0,1,0]
	v_pk_fma_f32 v[50:51], v[24:25], v[40:41], v[50:51] op_sel:[0,1,0]
	s_waitcnt lgkmcnt(1)
	v_pk_fma_f32 v[24:25], v[28:29], v[40:41], v[36:37] op_sel_hi:[1,0,1]
	v_pk_fma_f32 v[26:27], v[30:31], v[40:41], v[38:39] op_sel_hi:[1,0,1]
	s_waitcnt lgkmcnt(0)
	v_pk_fma_f32 v[32:33], v[32:33], v[40:41], v[24:25] op_sel:[0,1,0]
	v_pk_fma_f32 v[34:35], v[34:35], v[40:41], v[26:27] op_sel:[0,1,0]
	ds_read_b128 v[24:27], v128 offset:11264
	ds_read_b128 v[28:31], v128 offset:15360
	ds_read_b128 v[130:133], v128 offset:44032
	ds_read_b128 v[134:137], v128 offset:48128
	s_waitcnt lgkmcnt(3)
	v_pk_fma_f32 v[20:21], v[24:25], v[42:43], v[20:21] op_sel_hi:[1,0,1]
	v_pk_fma_f32 v[24:25], v[26:27], v[42:43], v[44:45] op_sel_hi:[1,0,1]
	s_waitcnt lgkmcnt(2)
	v_pk_fma_f32 v[20:21], v[28:29], v[42:43], v[20:21] op_sel:[0,1,0]
	v_pk_fma_f32 v[36:37], v[30:31], v[42:43], v[24:25] op_sel:[0,1,0]
	ds_read_b128 v[24:27], v129 offset:11264
	ds_read_b128 v[28:31], v129 offset:15360
	s_waitcnt lgkmcnt(3)
	v_pk_fma_f32 v[130:131], v[130:131], v[42:43], v[48:49] op_sel_hi:[1,0,1]
	v_pk_fma_f32 v[132:133], v[132:133], v[42:43], v[46:47] op_sel_hi:[1,0,1]
	s_waitcnt lgkmcnt(2)
	v_pk_fma_f32 v[40:41], v[134:135], v[42:43], v[130:131] op_sel:[0,1,0]
	v_pk_fma_f32 v[38:39], v[136:137], v[42:43], v[132:133] op_sel:[0,1,0]
	ds_read_b128 v[130:133], v129 offset:44032
	ds_read_b128 v[134:137], v129 offset:48128
	s_waitcnt lgkmcnt(3)
	v_pk_fma_f32 v[24:25], v[24:25], v[42:43], v[50:51] op_sel_hi:[1,0,1]
	v_pk_fma_f32 v[26:27], v[26:27], v[42:43], v[52:53] op_sel_hi:[1,0,1]
	s_waitcnt lgkmcnt(2)
	v_pk_fma_f32 v[46:47], v[28:29], v[42:43], v[24:25] op_sel:[0,1,0]
	v_pk_fma_f32 v[44:45], v[30:31], v[42:43], v[26:27] op_sel:[0,1,0]
	ds_read_b128 v[24:27], v128 offset:19456
	ds_read_b128 v[28:31], v128 offset:23552
	s_waitcnt lgkmcnt(3)
	v_pk_fma_f32 v[130:131], v[130:131], v[42:43], v[32:33] op_sel_hi:[1,0,1]
	v_pk_fma_f32 v[132:133], v[132:133], v[42:43], v[34:35] op_sel_hi:[1,0,1]
	s_waitcnt lgkmcnt(2)
; #define LAS __attribute__((address_space(3)))
; __device__ __forceinline__ unsigned cvt_pk_bf16(float lo, float hi) { const f32x2 v = {lo, hi}; const bf16x2_t b = __builtin_convertvector(v, bf16x2_t); return __builtin_bit_cast(unsigned, b); }
; #define H_MLOAD(dst, jj) do { dst[0] = *(const f32x4*)(gp + (jj) * 512); dst[1] = *(const f32x4*)(gp + (jj) * 512 + 4); dst[2] = *(const f32x4*)(m + 4 * DM + (jj) * 512); dst[3] = *(const f32x4*)(m + 4 * DM + (jj) * 512 + 4); \
;             dst[4] = *(const f32x4*)(m + 3 * DM + (jj) * 512); dst[5] = *(const f32x4*)(m + 3 * DM + (jj) * 512 + 4); } while (0)
; __device__ __forceinline__ void ph_norm2_router(const Params& p, int l, LAS unsigned char* lds) {
;     ...
;         for (int j = 0; j < 4; ++j) {
;             if (j < 3) H_MLOAD(mv[(j + 1) & 1], j + 1);
;             const f32x4 ga = mv[j & 1][0], gb = mv[j & 1][1], sa = mv[j & 1][2], sb = mv[j & 1][3], ha = mv[j & 1][4], hb = mv[j & 1][5];
;             float y[8];
; #pragma unroll
;             for (int i = 0; i < 8; ++i) y[i] = x[j][i] * rinv * (i < 4 ? ga[i] : gb[i - 4]) * (1.0f + (i < 4 ? sa[i] : sb[i - 4])) + (i < 4 ? ha[i] : hb[i - 4]);
;             u32x4 h; h.x = cvt_pk_bf16(y[0], y[1]); h.y = cvt_pk_bf16(y[2], y[3]); h.z = cvt_pk_bf16(y[4], y[5]); h.w = cvt_pk_bf16(y[6], y[7]);
;             *(u32x4*)(orow + j * 512) = h;
; #pragma unroll
;             for (int i2 = 0; i2 < 8; i2 += 2) {
; #pragma unroll
;                 for (int e4 = 0; e4 < 4; ++e4) { const f32x4 w0 = *(const LAS f32x4*)(lds + (size_t)(((e4 * 8 + i2) * 256 + j * 64 + lane) * 16)); const f32x4 w1 = *(const LAS f32x4*)(lds + (size_t)(((e4 * 8 + i2 + 1) * 256 + j * 64 + lane) * 16));
;                     lg[e4] = __builtin_elementwise_fma(w0, (f32x4){y[i2], y[i2], y[i2], y[i2]}, lg[e4]); lg[e4] = __builtin_elementwise_fma(w1, (f32x4){y[i2 + 1], y[i2 + 1], y[i2 + 1], y[i2 + 1]}, lg[e4]); }
;                 __builtin_amdgcn_sched_barrier(0); } }
;     ...
;         for (int e = 0; e < 8; ++e) { const float lo = lg[e >> 2][e & 3], hi_ = lg[(e + 8) >> 2][e & 3]; const float snd = (lane & 32) ? lo : hi_, kp = (lane & 32) ? hi_ : lo; v8[e] = kp + __shfl_xor(snd, 32); }
; #pragma unroll
;         for (int e = 0; e < 4; ++e) { const float snd = (lane & 16) ? v8[e] : v8[e + 4], kp = (lane & 16) ? v8[e + 4] : v8[e]; v4[e] = kp + __shfl_xor(snd, 16); }
	v_pk_fma_f32 v[34:35], v[134:135], v[42:43], v[130:131] op_sel:[0,1,0]
	v_pk_fma_f32 v[32:33], v[136:137], v[42:43], v[132:133] op_sel:[0,1,0]
	ds_read_b128 v[130:133], v128 offset:52224
	ds_read_b128 v[134:137], v128 offset:56320
	s_waitcnt lgkmcnt(3)
	v_pk_fma_f32 v[20:21], v[24:25], v[22:23], v[20:21] op_sel_hi:[1,0,1]
	v_pk_fma_f32 v[24:25], v[26:27], v[22:23], v[36:37] op_sel_hi:[1,0,1]
	s_waitcnt lgkmcnt(2)
	v_pk_fma_f32 v[42:43], v[28:29], v[22:23], v[20:21] op_sel:[0,1,0]
	v_pk_fma_f32 v[36:37], v[30:31], v[22:23], v[24:25] op_sel:[0,1,0]
	ds_read_b128 v[24:27], v129 offset:19456
	ds_read_b128 v[28:31], v129 offset:23552
	s_waitcnt lgkmcnt(3)
	v_pk_fma_f32 v[20:21], v[130:131], v[22:23], v[40:41] op_sel_hi:[1,0,1]
	v_pk_fma_f32 v[130:131], v[132:133], v[22:23], v[38:39] op_sel_hi:[1,0,1]
	s_waitcnt lgkmcnt(2)
	v_pk_fma_f32 v[40:41], v[134:135], v[22:23], v[20:21] op_sel:[0,1,0]
	v_pk_fma_f32 v[38:39], v[136:137], v[22:23], v[130:131] op_sel:[0,1,0]
	s_waitcnt lgkmcnt(1)
	v_pk_fma_f32 v[20:21], v[24:25], v[22:23], v[46:47] op_sel_hi:[1,0,1]
	v_pk_fma_f32 v[24:25], v[26:27], v[22:23], v[44:45] op_sel_hi:[1,0,1]
	s_waitcnt lgkmcnt(0)
	v_pk_fma_f32 v[46:47], v[28:29], v[22:23], v[20:21] op_sel:[0,1,0]
	v_pk_fma_f32 v[44:45], v[30:31], v[22:23], v[24:25] op_sel:[0,1,0]
	ds_read_b128 v[24:27], v129 offset:52224
	ds_read_b128 v[28:31], v129 offset:56320
	ds_read_b128 v[130:133], v128 offset:27648
	ds_read_b128 v[134:137], v128 offset:31744
	s_waitcnt lgkmcnt(3)
	v_pk_fma_f32 v[20:21], v[24:25], v[22:23], v[34:35] op_sel_hi:[1,0,1]
	v_pk_fma_f32 v[24:25], v[26:27], v[22:23], v[32:33] op_sel_hi:[1,0,1]
	s_waitcnt lgkmcnt(2)
	v_pk_fma_f32 v[28:29], v[28:29], v[22:23], v[20:21] op_sel:[0,1,0]
	v_pk_fma_f32 v[30:31], v[30:31], v[22:23], v[24:25] op_sel:[0,1,0]
	ds_read_b128 v[20:23], v128 offset:60416
	ds_read_b128 v[24:27], v128 offset:64512
	s_waitcnt lgkmcnt(3)
	v_pk_fma_f32 v[130:131], v[130:131], v[18:19], v[42:43] op_sel_hi:[1,0,1]
	v_pk_fma_f32 v[132:133], v[132:133], v[18:19], v[36:37] op_sel_hi:[1,0,1]
	s_waitcnt lgkmcnt(2)
	v_pk_fma_f32 v[34:35], v[134:135], v[18:19], v[130:131] op_sel:[0,1,0]
	v_pk_fma_f32 v[32:33], v[136:137], v[18:19], v[132:133] op_sel:[0,1,0]
	ds_read_b128 v[130:133], v129 offset:27648
	ds_read_b128 v[134:137], v129 offset:31744
	s_waitcnt lgkmcnt(3)
	v_pk_fma_f32 v[20:21], v[20:21], v[18:19], v[40:41] op_sel_hi:[1,0,1]
	v_pk_fma_f32 v[22:23], v[22:23], v[18:19], v[38:39] op_sel_hi:[1,0,1]
	s_waitcnt lgkmcnt(2)
	v_pk_fma_f32 v[38:39], v[24:25], v[18:19], v[20:21] op_sel:[0,1,0]
	v_pk_fma_f32 v[36:37], v[26:27], v[18:19], v[22:23] op_sel:[0,1,0]
	ds_read_b128 v[20:23], v129 offset:60416
	ds_read_b128 v[24:27], v129 offset:64512
	s_waitcnt lgkmcnt(3)
	v_pk_fma_f32 v[130:131], v[130:131], v[18:19], v[46:47] op_sel_hi:[1,0,1]
	v_pk_fma_f32 v[132:133], v[132:133], v[18:19], v[44:45] op_sel_hi:[1,0,1]
	s_waitcnt lgkmcnt(2)
	v_pk_fma_f32 v[42:43], v[134:135], v[18:19], v[130:131] op_sel:[0,1,0]
	v_pk_fma_f32 v[40:41], v[136:137], v[18:19], v[132:133] op_sel:[0,1,0]
	s_waitcnt lgkmcnt(1)
	v_pk_fma_f32 v[20:21], v[20:21], v[18:19], v[28:29] op_sel_hi:[1,0,1]
	v_pk_fma_f32 v[22:23], v[22:23], v[18:19], v[30:31] op_sel_hi:[1,0,1]
	s_waitcnt lgkmcnt(0)
	v_pk_fma_f32 v[22:23], v[26:27], v[18:19], v[22:23] op_sel:[0,1,0]
	v_pk_fma_f32 v[18:19], v[24:25], v[18:19], v[20:21] op_sel:[0,1,0]
	v_cndmask_b32_e64 v20, v34, v42, s[36:37]
	ds_bpermute_b32 v20, v122, v20
	v_cndmask_b32_e64 v21, v42, v34, s[36:37]
	v_cndmask_b32_e64 v24, v43, v35, s[36:37]
	v_cndmask_b32_e64 v25, v40, v32, s[36:37]
	v_cndmask_b32_e64 v26, v41, v33, s[36:37]
	s_waitcnt lgkmcnt(0)
	v_add_f32_e32 v20, v21, v20
	v_cndmask_b32_e64 v21, v35, v43, s[36:37]
	ds_bpermute_b32 v21, v122, v21
	s_waitcnt lgkmcnt(0)
	v_add_f32_e32 v21, v24, v21
	v_cndmask_b32_e64 v24, v32, v40, s[36:37]
	ds_bpermute_b32 v24, v122, v24
	s_waitcnt lgkmcnt(0)
	v_add_f32_e32 v24, v25, v24
	v_cndmask_b32_e64 v25, v33, v41, s[36:37]
	ds_bpermute_b32 v25, v122, v25
	s_waitcnt lgkmcnt(0)
; __device__ __forceinline__ void ph_norm2_router(const Params& p, int l, LAS unsigned char* lds) {
;     ...
;         for (int e = 0; e < 8; ++e) { const float lo = lg[e >> 2][e & 3], hi_ = lg[(e + 8) >> 2][e & 3]; const float snd = (lane & 32) ? lo : hi_, kp = (lane & 32) ? hi_ : lo; v8[e] = kp + __shfl_xor(snd, 32); }
; #pragma unroll
;         for (int e = 0; e < 4; ++e) { const float snd = (lane & 16) ? v8[e] : v8[e + 4], kp = (lane & 16) ? v8[e + 4] : v8[e]; v4[e] = kp + __shfl_xor(snd, 16); }
; #pragma unroll
;         for (int e = 0; e < 2; ++e) { const float snd = (lane & 8) ? v4[e] : v4[e + 2], kp = (lane & 8) ? v4[e + 2] : v4[e]; v2[e] = kp + __shfl_xor(snd, 8); }
;         { const float snd = (lane & 4) ? v2[0] : v2[1], kp = (lane & 4) ? v2[1] : v2[0]; v1 = kp + __shfl_xor(snd, 4); }
;         v1 += __shfl_xor(v1, 1); v1 += __shfl_xor(v1, 2);
;         float mx = v1; mx = fmaxf(mx, __shfl_xor(mx, 4)); mx = fmaxf(mx, __shfl_xor(mx, 8)); mx = fmaxf(mx, __shfl_xor(mx, 16)); mx = fmaxf(mx, __shfl_xor(mx, 32));
;         const float ex = __expf(v1 - mx); float se = ex; se += __shfl_xor(se, 4); se += __shfl_xor(se, 8); se += __shfl_xor(se, 16); se += __shfl_xor(se, 32);
;         if ((lane & 3) == 0) ((float*)(ws + WS_AFF))[(size_t)row * 16 + (lane >> 2)] = ex / se;
	v_add_f32_e32 v25, v26, v25
	v_cndmask_b32_e64 v26, v38, v18, s[36:37]
	ds_bpermute_b32 v26, v122, v26
	v_cndmask_b32_e64 v18, v18, v38, s[36:37]
	s_waitcnt lgkmcnt(0)
	v_add_f32_e32 v18, v18, v26
	v_cndmask_b32_e64 v26, v39, v19, s[36:37]
	ds_bpermute_b32 v26, v122, v26
	v_cndmask_b32_e64 v19, v19, v39, s[36:37]
	s_waitcnt lgkmcnt(0)
	v_add_f32_e32 v19, v19, v26
	v_cndmask_b32_e64 v26, v36, v22, s[36:37]
	ds_bpermute_b32 v26, v122, v26
	v_cndmask_b32_e64 v22, v22, v36, s[36:37]
	s_waitcnt lgkmcnt(0)
	v_add_f32_e32 v22, v22, v26
	v_cndmask_b32_e64 v26, v37, v23, s[36:37]
	ds_bpermute_b32 v26, v122, v26
	v_cndmask_b32_e64 v23, v23, v37, s[36:37]
	s_waitcnt lgkmcnt(0)
	v_add_f32_e32 v23, v23, v26
	v_cndmask_b32_e64 v26, v20, v18, s[38:39]
	v_cndmask_b32_e64 v18, v18, v20, s[38:39]
	ds_bpermute_b32 v20, v123, v26
	s_waitcnt lgkmcnt(0)
	v_add_f32_e32 v18, v18, v20
	v_cndmask_b32_e64 v20, v21, v19, s[38:39]
	ds_bpermute_b32 v20, v123, v20
	v_cndmask_b32_e64 v19, v19, v21, s[38:39]
	v_cndmask_b32_e64 v21, v22, v24, s[38:39]
	s_waitcnt lgkmcnt(0)
	v_add_f32_e32 v19, v19, v20
	v_cndmask_b32_e64 v20, v24, v22, s[38:39]
	ds_bpermute_b32 v20, v123, v20
	v_cndmask_b32_e64 v22, v23, v25, s[38:39]
	s_waitcnt lgkmcnt(0)
	v_add_f32_e32 v20, v21, v20
	v_cndmask_b32_e64 v21, v25, v23, s[38:39]
	ds_bpermute_b32 v21, v123, v21
	s_waitcnt lgkmcnt(0)
	v_add_f32_e32 v21, v22, v21
	v_cndmask_b32_e64 v22, v18, v20, s[40:41]
	v_cndmask_b32_e64 v18, v20, v18, s[40:41]
	s_nop 1
	v_mov_b32_dpp v20, v22 row_ror:8 row_mask:0xf bank_mask:0xf
	s_waitcnt lgkmcnt(0)
	v_add_f32_e32 v18, v18, v20
	v_cndmask_b32_e64 v20, v19, v21, s[40:41]
	ds_bpermute_b32 v20, v124, v20
	v_cndmask_b32_e64 v19, v21, v19, s[40:41]
	s_waitcnt lgkmcnt(0)
	v_add_f32_e32 v19, v19, v20
	v_cndmask_b32_e64 v20, v18, v19, s[42:43]
	v_cndmask_b32_e64 v18, v19, v18, s[42:43]
	s_nop 1
	v_mov_b32_dpp v19, v20 row_shl:4 row_mask:0xf bank_mask:0x5
	v_mov_b32_dpp v19, v20 row_shr:4 row_mask:0xf bank_mask:0xa
	s_waitcnt lgkmcnt(0)
	v_add_f32_e32 v18, v18, v19
	s_nop 1
	v_mov_b32_dpp v19, v18 quad_perm:[1,0,3,2] row_mask:0xf bank_mask:0xf
	s_waitcnt lgkmcnt(0)
	v_add_f32_e32 v18, v18, v19
	s_nop 1
	v_mov_b32_dpp v19, v18 quad_perm:[2,3,0,1] row_mask:0xf bank_mask:0xf
	s_waitcnt lgkmcnt(0)
	v_add_f32_e32 v18, v18, v19
	s_nop 1
	v_mov_b32_dpp v19, v18 row_shl:4 row_mask:0xf bank_mask:0x5
	v_mov_b32_dpp v19, v18 row_shr:4 row_mask:0xf bank_mask:0xa
	s_waitcnt lgkmcnt(0)
	v_max_f32_e32 v19, v19, v19
	v_max_f32_e32 v19, v18, v19
	s_nop 1
	v_mov_b32_dpp v20, v19 row_ror:8 row_mask:0xf bank_mask:0xf
	s_waitcnt lgkmcnt(0)
	v_max_f32_e32 v20, v20, v20
	v_max_f32_e32 v19, v19, v20
	v_mov_b32_e32 v20, v19
	s_nop 1
	v_permlane16_swap_b32_e32 v20, v19
	s_waitcnt lgkmcnt(0)
	v_max_f32_e32 v20, v20, v20
	v_max_f32_e32 v19, v19, v20
	v_mov_b32_e32 v20, v19
	s_nop 1
	v_permlane32_swap_b32_e32 v20, v19
	s_waitcnt lgkmcnt(0)
	v_max_f32_e32 v20, v20, v20
	v_max_f32_e32 v19, v19, v20
	v_sub_f32_e32 v18, v18, v19
	v_mul_f32_e32 v18, 0x3fb8aa3b, v18
	v_exp_f32_e32 v18, v18
	s_nop 1
	v_mov_b32_dpp v19, v18 row_shl:4 row_mask:0xf bank_mask:0x5
	v_mov_b32_dpp v19, v18 row_shr:4 row_mask:0xf bank_mask:0xa
	s_waitcnt lgkmcnt(0)
	v_add_f32_e32 v19, v18, v19
	s_nop 1
	v_mov_b32_dpp v20, v19 row_ror:8 row_mask:0xf bank_mask:0xf
	s_waitcnt lgkmcnt(0)
	v_add_f32_e32 v19, v19, v20
	v_mov_b32_e32 v20, v19
	s_nop 1
	v_permlane16_swap_b32_e32 v20, v19
	s_waitcnt lgkmcnt(0)
	v_add_f32_e32 v19, v19, v20
	ds_bpermute_b32 v20, v122, v19
	s_and_saveexec_b64 s[0:1], s[44:45]
	s_cbranch_execz .LBB0_1757
	s_waitcnt lgkmcnt(0)
	v_add_f32_e32 v19, v19, v20
	v_div_scale_f32 v20, s[14:15], v19, v19, v18
	v_rcp_f32_e32 v21, v20
	v_div_scale_f32 v22, vcc, v18, v19, v18
	v_fma_f32 v23, -v20, v21, 1.0
	v_fmac_f32_e32 v21, v23, v21
	v_mul_f32_e32 v23, v22, v21
	v_fma_f32 v24, -v20, v23, v22
	v_fmac_f32_e32 v23, v24, v21
	v_fma_f32 v20, -v20, v23, v22
	v_div_fmas_f32 v20, v20, v21, v23
	v_div_fixup_f32 v20, v20, v19, v18
	v_lshlrev_b64 v[18:19], 6, v[80:81]
	v_lshl_add_u64 v[18:19], v[74:75], 0, v[18:19]
	global_store_dword v[18:19], v20, off
	s_branch .LBB0_1757
